# P6: warm the gate rows mid() reads with 4 one-dword loads per K-loop phase in the two trips before the K midpoint; counted waits widened to vmcnt(12) while those are in flight
# speedup vs baseline: 1.0051x; 1.0003x over previous
.LBB0_674:
	v_add_u32_e32 v162, s52, v167
	ds_read_b128 v[130:133], v162
	ds_read_b128 v[134:137], v162 offset:1024
	ds_read_b128 v[172:175], v162 offset:2048
	ds_read_b128 v[176:179], v162 offset:3072
	v_add_u32_e32 v162, s53, v167
	s_add_u32 s28, s24, s26
	ds_read_b128 v[180:183], v162
	ds_read_b128 v[184:187], v162 offset:1024
	ds_read_b128 v[188:191], v162 offset:2048
	ds_read_b128 v[192:195], v162 offset:3072
	s_addc_u32 s29, s25, s27
	s_add_u32 s28, s28, 0x100
	s_addc_u32 s29, s29, 0
	s_add_u32 s62, s59, s26
	s_addc_u32 s63, s60, s27
	s_cmpk_eq_i32 s26, 0x900
	s_cselect_b32 s31, s5, s29
	s_cselect_b32 s30, s4, s28
	s_cselect_b32 s29, s23, s63
	s_cselect_b32 s28, s22, s62
	v_lshl_add_u64 v[162:163], v[158:159], 0, s[26:27]
	s_add_i32 m0, s39, 0xc000
	ds_read_b128 v[196:199], v168
	ds_read_b128 v[200:203], v168 offset:1024
	ds_read_b128 v[204:207], v168 offset:2048
	ds_read_b128 v[208:211], v168 offset:3072
	ds_read_b128 v[212:215], v168 offset:4096
	ds_read_b128 v[216:219], v168 offset:5120
	ds_read_b128 v[220:223], v168 offset:6144
	ds_read_b128 v[224:227], v168 offset:7168
	global_load_lds_dwordx4 v[162:163], off
	v_lshl_add_u64 v[162:163], v[160:161], 0, s[26:27]
	s_add_i32 m0, s39, 0xe000
	s_nop 0
	global_load_lds_dwordx4 v[162:163], off
	s_waitcnt vmcnt(12)
	s_cmpk_lg_i32 s26, 0x100
	s_cbranch_scc0 .Lp6pf_w0
	s_waitcnt vmcnt(8)
.Lp6pf_w0:
	s_waitcnt lgkmcnt(0)
	s_barrier
	s_setprio 1
	s_waitcnt lgkmcnt(0)
	v_mfma_scale_f32_16x16x128_f8f6f4 v[126:129], v[130:137], v[196:203], v[126:129], v169, v169 op_sel_hi:[0,0,0]
	v_mfma_scale_f32_16x16x128_f8f6f4 v[122:125], v[172:179], v[196:203], v[122:125], v169, v169 op_sel_hi:[0,0,0]
	v_mfma_scale_f32_16x16x128_f8f6f4 v[110:113], v[130:137], v[204:211], v[110:113], v169, v169 op_sel_hi:[0,0,0]
	v_mfma_scale_f32_16x16x128_f8f6f4 v[106:109], v[172:179], v[204:211], v[106:109], v169, v169 op_sel_hi:[0,0,0]
	v_mfma_scale_f32_16x16x128_f8f6f4 v[94:97], v[130:137], v[212:219], v[94:97], v169, v169 op_sel_hi:[0,0,0]
	v_mfma_scale_f32_16x16x128_f8f6f4 v[90:93], v[172:179], v[212:219], v[90:93], v169, v169 op_sel_hi:[0,0,0]
	v_mfma_scale_f32_16x16x128_f8f6f4 v[78:81], v[130:137], v[220:227], v[78:81], v169, v169 op_sel_hi:[0,0,0]
	v_mfma_scale_f32_16x16x128_f8f6f4 v[74:77], v[172:179], v[220:227], v[74:77], v169, v169 op_sel_hi:[0,0,0]
	s_setprio 0
	s_setprio 1
	v_mfma_scale_f32_16x16x128_f8f6f4 v[118:121], v[180:187], v[196:203], v[118:121], v169, v169 op_sel_hi:[0,0,0]
	v_mfma_scale_f32_16x16x128_f8f6f4 v[114:117], v[188:195], v[196:203], v[114:117], v169, v169 op_sel_hi:[0,0,0]
	v_mfma_scale_f32_16x16x128_f8f6f4 v[102:105], v[180:187], v[204:211], v[102:105], v169, v169 op_sel_hi:[0,0,0]
	v_mfma_scale_f32_16x16x128_f8f6f4 v[98:101], v[188:195], v[204:211], v[98:101], v169, v169 op_sel_hi:[0,0,0]
	v_mfma_scale_f32_16x16x128_f8f6f4 v[86:89], v[180:187], v[212:219], v[86:89], v169, v169 op_sel_hi:[0,0,0]
	v_mfma_scale_f32_16x16x128_f8f6f4 v[82:85], v[188:195], v[212:219], v[82:85], v169, v169 op_sel_hi:[0,0,0]
	v_mfma_scale_f32_16x16x128_f8f6f4 v[70:73], v[180:187], v[220:227], v[70:73], v169, v169 op_sel_hi:[0,0,0]
	v_mfma_scale_f32_16x16x128_f8f6f4 v[66:69], v[188:195], v[220:227], v[66:69], v169, v169 op_sel_hi:[0,0,0]
	s_cmpk_lt_u32 s26, 0x200
	s_cbranch_scc0 .Lp6pf_skip_0
	v_mov_b32_e32 v248, s26
	v_lshrrev_b32_e32 v248, 1, v248
	v_add3_u32 v248, s57, v1, v248
	v_mul_lo_u32 v248, v248, s50
	v_lshl_add_u32 v250, v166, 3, s58
	v_lshl_add_u32 v248, v250, 1, v248
	v_add_u32_e32 v249, 0x3c00, v248
	v_add_u32_e32 v250, 0x4c00, v248
	global_load_dword v244, v249, s[8:9]
	global_load_dword v245, v249, s[8:9] offset:256
	global_load_dword v246, v250, s[8:9]
	global_load_dword v247, v250, s[8:9] offset:256
.Lp6pf_skip_0:
	s_setprio 0
	s_barrier
	s_add_i32 s62, s52, s38
	v_lshl_add_u64 v[162:163], s[28:29], 0, v[138:139]
	s_mov_b32 m0, s62
	ds_read_b128 v[196:199], v168 offset:16384
	ds_read_b128 v[200:203], v168 offset:17408
	ds_read_b128 v[204:207], v168 offset:18432
	ds_read_b128 v[208:211], v168 offset:19456
	ds_read_b128 v[212:215], v168 offset:20480
	ds_read_b128 v[216:219], v168 offset:21504
	ds_read_b128 v[220:223], v168 offset:22528
	ds_read_b128 v[224:227], v168 offset:23552
	global_load_lds_dwordx4 v[162:163], off
	s_add_i32 m0, s62, 0x2000
	s_add_u32 s62, s28, 0x50000
	v_lshl_add_u64 v[164:165], s[28:29], 0, v[140:141]
	s_addc_u32 s63, s29, 0
	s_add_i32 s64, s53, s38
	global_load_lds_dwordx4 v[164:165], off
	v_lshl_add_u64 v[228:229], s[62:63], 0, v[138:139]
	s_mov_b32 m0, s64
	v_lshl_add_u64 v[230:231], s[30:31], 0, v[144:145]
	global_load_lds_dwordx4 v[228:229], off
	v_lshl_add_u64 v[228:229], s[62:63], 0, v[140:141]
	s_add_i32 m0, s64, 0x2000
	s_nop 0
	global_load_lds_dwordx4 v[228:229], off
	v_lshl_add_u64 v[228:229], s[30:31], 0, v[142:143]
	s_mov_b32 m0, s39
	s_nop 0
	global_load_lds_dwordx4 v[228:229], off
	s_mov_b32 m0, s40
	s_nop 0
	global_load_lds_dwordx4 v[230:231], off
	s_waitcnt vmcnt(12)
	s_cmpk_lt_u32 s26, 0x200
	s_cbranch_scc1 .Lp6pf_w1
	s_waitcnt vmcnt(8)
.Lp6pf_w1:
	s_waitcnt lgkmcnt(0)
	s_barrier
	s_setprio 1
	s_waitcnt lgkmcnt(0)
	v_mfma_scale_f32_16x16x128_f8f6f4 v[62:65], v[130:137], v[196:203], v[62:65], v169, v169 op_sel_hi:[0,0,0]
	v_mfma_scale_f32_16x16x128_f8f6f4 v[58:61], v[172:179], v[196:203], v[58:61], v169, v169 op_sel_hi:[0,0,0]
	v_mfma_scale_f32_16x16x128_f8f6f4 v[46:49], v[130:137], v[204:211], v[46:49], v169, v169 op_sel_hi:[0,0,0]
	v_mfma_scale_f32_16x16x128_f8f6f4 v[42:45], v[172:179], v[204:211], v[42:45], v169, v169 op_sel_hi:[0,0,0]
	v_mfma_scale_f32_16x16x128_f8f6f4 v[30:33], v[130:137], v[212:219], v[30:33], v169, v169 op_sel_hi:[0,0,0]
	v_mfma_scale_f32_16x16x128_f8f6f4 v[26:29], v[172:179], v[212:219], v[26:29], v169, v169 op_sel_hi:[0,0,0]
	v_mfma_scale_f32_16x16x128_f8f6f4 v[6:9], v[130:137], v[220:227], v[6:9], v169, v169 op_sel_hi:[0,0,0]
	v_mfma_scale_f32_16x16x128_f8f6f4 v[2:5], v[172:179], v[220:227], v[2:5], v169, v169 op_sel_hi:[0,0,0]
	s_setprio 0
	s_setprio 1
	v_mfma_scale_f32_16x16x128_f8f6f4 v[50:53], v[180:187], v[196:203], v[50:53], v169, v169 op_sel_hi:[0,0,0]
	v_mfma_scale_f32_16x16x128_f8f6f4 v[54:57], v[188:195], v[196:203], v[54:57], v169, v169 op_sel_hi:[0,0,0]
	v_mfma_scale_f32_16x16x128_f8f6f4 v[34:37], v[180:187], v[204:211], v[34:37], v169, v169 op_sel_hi:[0,0,0]
	v_mfma_scale_f32_16x16x128_f8f6f4 v[38:41], v[188:195], v[204:211], v[38:41], v169, v169 op_sel_hi:[0,0,0]
	v_mfma_scale_f32_16x16x128_f8f6f4 v[18:21], v[180:187], v[212:219], v[18:21], v169, v169 op_sel_hi:[0,0,0]
	v_mfma_scale_f32_16x16x128_f8f6f4 v[22:25], v[188:195], v[212:219], v[22:25], v169, v169 op_sel_hi:[0,0,0]
	v_mfma_scale_f32_16x16x128_f8f6f4 v[10:13], v[180:187], v[220:227], v[10:13], v169, v169 op_sel_hi:[0,0,0]
	v_mfma_scale_f32_16x16x128_f8f6f4 v[14:17], v[188:195], v[220:227], v[14:17], v169, v169 op_sel_hi:[0,0,0]
	s_cmpk_lt_u32 s26, 0x200
	s_cbranch_scc0 .Lp6pf_skip_1
	v_mov_b32_e32 v248, s26
	v_lshrrev_b32_e32 v248, 1, v248
	v_add3_u32 v248, s57, v1, v248
	v_add_u32_e32 v248, 16, v248
	v_mul_lo_u32 v248, v248, s50
	v_lshl_add_u32 v250, v166, 3, s58
	v_lshl_add_u32 v248, v250, 1, v248
	v_add_u32_e32 v249, 0x3c00, v248
	v_add_u32_e32 v250, 0x4c00, v248
	global_load_dword v244, v249, s[8:9]
	global_load_dword v245, v249, s[8:9] offset:256
	global_load_dword v246, v250, s[8:9]
	global_load_dword v247, v250, s[8:9] offset:256
.Lp6pf_skip_1:
	s_setprio 0
	s_barrier
	s_add_i32 s62, 0, 0x18000
	v_add_u32_e32 v171, s62, v167
	s_add_i32 s63, 0, 0x1c000
	ds_read_b128 v[130:133], v171
	ds_read_b128 v[134:137], v171 offset:1024
	ds_read_b128 v[172:175], v171 offset:2048
	ds_read_b128 v[176:179], v171 offset:3072
	v_add_u32_e32 v171, s63, v167
	ds_read_b128 v[180:183], v171
	ds_read_b128 v[184:187], v171 offset:1024
	ds_read_b128 v[188:191], v171 offset:2048
	ds_read_b128 v[192:195], v171 offset:3072
	s_mov_b32 m0, s41
	v_lshl_add_u64 v[232:233], s[30:31], 0, v[146:147]
	ds_read_b128 v[196:199], v168 offset:32768
	ds_read_b128 v[200:203], v168 offset:33792
	ds_read_b128 v[204:207], v168 offset:34816
	ds_read_b128 v[208:211], v168 offset:35840
	ds_read_b128 v[212:215], v168 offset:36864
	ds_read_b128 v[216:219], v168 offset:37888
	ds_read_b128 v[220:223], v168 offset:38912
	ds_read_b128 v[224:227], v168 offset:39936
	global_load_lds_dwordx4 v[232:233], off
	v_lshl_add_u64 v[232:233], s[30:31], 0, v[148:149]
	s_mov_b32 m0, s42
	s_nop 0
	global_load_lds_dwordx4 v[232:233], off
	s_waitcnt vmcnt(12)
	s_cmpk_lt_u32 s26, 0x200
	s_cbranch_scc1 .Lp6pf_w2
	s_waitcnt vmcnt(8)
.Lp6pf_w2:
	s_waitcnt lgkmcnt(0)
	s_barrier
	s_setprio 1
	s_waitcnt lgkmcnt(0)
	v_mfma_scale_f32_16x16x128_f8f6f4 v[126:129], v[130:137], v[196:203], v[126:129], v169, v169 op_sel_hi:[0,0,0]
	v_mfma_scale_f32_16x16x128_f8f6f4 v[122:125], v[172:179], v[196:203], v[122:125], v169, v169 op_sel_hi:[0,0,0]
	v_mfma_scale_f32_16x16x128_f8f6f4 v[110:113], v[130:137], v[204:211], v[110:113], v169, v169 op_sel_hi:[0,0,0]
	v_mfma_scale_f32_16x16x128_f8f6f4 v[106:109], v[172:179], v[204:211], v[106:109], v169, v169 op_sel_hi:[0,0,0]
	v_mfma_scale_f32_16x16x128_f8f6f4 v[94:97], v[130:137], v[212:219], v[94:97], v169, v169 op_sel_hi:[0,0,0]
	v_mfma_scale_f32_16x16x128_f8f6f4 v[90:93], v[172:179], v[212:219], v[90:93], v169, v169 op_sel_hi:[0,0,0]
	v_mfma_scale_f32_16x16x128_f8f6f4 v[78:81], v[130:137], v[220:227], v[78:81], v169, v169 op_sel_hi:[0,0,0]
	v_mfma_scale_f32_16x16x128_f8f6f4 v[74:77], v[172:179], v[220:227], v[74:77], v169, v169 op_sel_hi:[0,0,0]
	s_setprio 0
	s_setprio 1
	v_mfma_scale_f32_16x16x128_f8f6f4 v[118:121], v[180:187], v[196:203], v[118:121], v169, v169 op_sel_hi:[0,0,0]
	v_mfma_scale_f32_16x16x128_f8f6f4 v[114:117], v[188:195], v[196:203], v[114:117], v169, v169 op_sel_hi:[0,0,0]
	v_mfma_scale_f32_16x16x128_f8f6f4 v[102:105], v[180:187], v[204:211], v[102:105], v169, v169 op_sel_hi:[0,0,0]
	v_mfma_scale_f32_16x16x128_f8f6f4 v[98:101], v[188:195], v[204:211], v[98:101], v169, v169 op_sel_hi:[0,0,0]
	v_mfma_scale_f32_16x16x128_f8f6f4 v[86:89], v[180:187], v[212:219], v[86:89], v169, v169 op_sel_hi:[0,0,0]
	v_mfma_scale_f32_16x16x128_f8f6f4 v[82:85], v[188:195], v[212:219], v[82:85], v169, v169 op_sel_hi:[0,0,0]
	v_mfma_scale_f32_16x16x128_f8f6f4 v[70:73], v[180:187], v[220:227], v[70:73], v169, v169 op_sel_hi:[0,0,0]
	v_mfma_scale_f32_16x16x128_f8f6f4 v[66:69], v[188:195], v[220:227], v[66:69], v169, v169 op_sel_hi:[0,0,0]
	s_cmpk_lt_u32 s26, 0x200
	s_cbranch_scc0 .Lp6pf_skip_2
	v_mov_b32_e32 v248, s26
	v_lshrrev_b32_e32 v248, 1, v248
	v_add3_u32 v248, s57, v1, v248
	v_add_u32_e32 v248, 32, v248
	v_mul_lo_u32 v248, v248, s50
	v_lshl_add_u32 v250, v166, 3, s58
	v_lshl_add_u32 v248, v250, 1, v248
	v_add_u32_e32 v249, 0x3c00, v248
	v_add_u32_e32 v250, 0x4c00, v248
	global_load_dword v244, v249, s[8:9]
	global_load_dword v245, v249, s[8:9] offset:256
	global_load_dword v246, v250, s[8:9]
	global_load_dword v247, v250, s[8:9] offset:256
.Lp6pf_skip_2:
	s_setprio 0
	s_barrier
	s_add_i32 s30, s62, s38
	v_lshl_add_u64 v[162:163], v[162:163], 0, s[12:13]
	s_mov_b32 m0, s30
	ds_read_b128 v[196:199], v168 offset:49152
	ds_read_b128 v[200:203], v168 offset:50176
	ds_read_b128 v[204:207], v168 offset:51200
	ds_read_b128 v[208:211], v168 offset:52224
	ds_read_b128 v[212:215], v168 offset:53248
	ds_read_b128 v[216:219], v168 offset:54272
	ds_read_b128 v[220:223], v168 offset:55296
	ds_read_b128 v[224:227], v168 offset:56320
	global_load_lds_dwordx4 v[162:163], off
	s_add_i32 m0, s30, 0x2000
	s_add_u32 s28, s28, 0x50080
	v_lshl_add_u64 v[162:163], v[164:165], 0, s[12:13]
	s_addc_u32 s29, s29, 0
	s_add_i32 s30, s63, s38
	global_load_lds_dwordx4 v[162:163], off
	v_lshl_add_u64 v[162:163], s[28:29], 0, v[138:139]
	s_mov_b32 m0, s30
	s_nop 0
	global_load_lds_dwordx4 v[162:163], off
	v_lshl_add_u64 v[162:163], s[28:29], 0, v[140:141]
	s_add_i32 m0, s30, 0x2000
	s_nop 0
	global_load_lds_dwordx4 v[162:163], off
	v_lshl_add_u64 v[162:163], v[228:229], 0, s[12:13]
	s_mov_b32 m0, s47
	s_nop 0
	global_load_lds_dwordx4 v[162:163], off
	v_lshl_add_u64 v[162:163], v[230:231], 0, s[12:13]
	s_mov_b32 m0, s48
	s_nop 0
	global_load_lds_dwordx4 v[162:163], off
	s_waitcnt vmcnt(12)
	s_cmpk_lt_u32 s26, 0x200
	s_cbranch_scc1 .Lp6pf_w3
	s_waitcnt vmcnt(8)
.Lp6pf_w3:
	s_waitcnt lgkmcnt(0)
	s_barrier
	s_setprio 1
	s_waitcnt lgkmcnt(0)
	v_mfma_scale_f32_16x16x128_f8f6f4 v[62:65], v[130:137], v[196:203], v[62:65], v169, v169 op_sel_hi:[0,0,0]
	v_mfma_scale_f32_16x16x128_f8f6f4 v[58:61], v[172:179], v[196:203], v[58:61], v169, v169 op_sel_hi:[0,0,0]
	v_mfma_scale_f32_16x16x128_f8f6f4 v[46:49], v[130:137], v[204:211], v[46:49], v169, v169 op_sel_hi:[0,0,0]
	v_mfma_scale_f32_16x16x128_f8f6f4 v[42:45], v[172:179], v[204:211], v[42:45], v169, v169 op_sel_hi:[0,0,0]
	v_mfma_scale_f32_16x16x128_f8f6f4 v[30:33], v[130:137], v[212:219], v[30:33], v169, v169 op_sel_hi:[0,0,0]
	v_mfma_scale_f32_16x16x128_f8f6f4 v[26:29], v[172:179], v[212:219], v[26:29], v169, v169 op_sel_hi:[0,0,0]
	v_mfma_scale_f32_16x16x128_f8f6f4 v[6:9], v[130:137], v[220:227], v[6:9], v169, v169 op_sel_hi:[0,0,0]
	v_mfma_scale_f32_16x16x128_f8f6f4 v[2:5], v[172:179], v[220:227], v[2:5], v169, v169 op_sel_hi:[0,0,0]
	s_setprio 0
	s_setprio 1
	v_mfma_scale_f32_16x16x128_f8f6f4 v[50:53], v[180:187], v[196:203], v[50:53], v169, v169 op_sel_hi:[0,0,0]
	v_mfma_scale_f32_16x16x128_f8f6f4 v[54:57], v[188:195], v[196:203], v[54:57], v169, v169 op_sel_hi:[0,0,0]
	v_mfma_scale_f32_16x16x128_f8f6f4 v[34:37], v[180:187], v[204:211], v[34:37], v169, v169 op_sel_hi:[0,0,0]
	v_mfma_scale_f32_16x16x128_f8f6f4 v[38:41], v[188:195], v[204:211], v[38:41], v169, v169 op_sel_hi:[0,0,0]
	v_mfma_scale_f32_16x16x128_f8f6f4 v[18:21], v[180:187], v[212:219], v[18:21], v169, v169 op_sel_hi:[0,0,0]
	v_mfma_scale_f32_16x16x128_f8f6f4 v[22:25], v[188:195], v[212:219], v[22:25], v169, v169 op_sel_hi:[0,0,0]
	v_mfma_scale_f32_16x16x128_f8f6f4 v[10:13], v[180:187], v[220:227], v[10:13], v169, v169 op_sel_hi:[0,0,0]
	v_mfma_scale_f32_16x16x128_f8f6f4 v[14:17], v[188:195], v[220:227], v[14:17], v169, v169 op_sel_hi:[0,0,0]
	s_cmpk_lt_u32 s26, 0x200
	s_cbranch_scc0 .Lp6pf_skip_3
	v_mov_b32_e32 v248, s26
	v_lshrrev_b32_e32 v248, 1, v248
	v_add3_u32 v248, s57, v1, v248
	v_add_u32_e32 v248, 48, v248
	v_mul_lo_u32 v248, v248, s50
	v_lshl_add_u32 v250, v166, 3, s58
	v_lshl_add_u32 v248, v250, 1, v248
	v_add_u32_e32 v249, 0x3c00, v248
	v_add_u32_e32 v250, 0x4c00, v248
	global_load_dword v244, v249, s[8:9]
	global_load_dword v245, v249, s[8:9] offset:256
	global_load_dword v246, v250, s[8:9]
	global_load_dword v247, v250, s[8:9] offset:256
.Lp6pf_skip_3:
	s_setprio 0
	s_barrier
	s_add_i32 s61, s61, 2
	s_add_u32 s26, s26, 0x100
	s_addc_u32 s27, s27, 0
	s_cmp_gt_u32 s61, 17
	s_cbranch_scc1 .LBB0_677
